# attn_ret: the eight carried-state staging loads put in flight together (own registers), LDS writes behind counted waits, on top of v90
# baseline (speedup 1.0000x reference)
.LBB0_1134:
	s_lshl_b32 s5, s14, 7
	s_lshl_b32 s6, s15, 5
	s_ashr_i32 s4, s4, 7
	s_or_b32 s5, s5, s6
	s_add_i32 s4, s5, s4
	s_ashr_i32 s5, s4, 31
	s_lshl_b64 s[4:5], s[4:5], 16
	s_add_u32 s4, s2, s4
	s_addc_u32 s5, s3, s5
	v_ashrrev_i32_e32 v76, 11, v209
	s_add_u32 s4, s4, 0x4b900000
	v_ashrrev_i32_e32 v77, 31, v76
	s_addc_u32 s5, s5, 0
	v_bfe_u32 v78, v209, 4, 7
	v_lshlrev_b64 v[68:69], 16, v[76:77]
	v_lshl_add_u64 v[70:71], s[4:5], 0, v[68:69]
	v_lshlrev_b32_e32 v68, 8, v78
	v_mov_b32_e32 v69, v3
	v_lshl_add_u64 v[70:71], v[70:71], 0, v[68:69]
	v_mov_b32_e32 v195, v3
	v_lshl_add_u64 v[70:71], v[70:71], 0, v[194:195]
	global_load_dwordx4 v[132:135], v[70:71], off
	v_mov_b32_e32 v70, s72
	s_mov_b32 s6, 0x8900
	v_mad_i32_i24 v71, v76, s6, v70
	v_mul_u32_u24_e32 v78, 0x110, v78
	v_ashrrev_i32_e32 v76, 11, v210
	v_add3_u32 v71, v71, v78, v194
	v_ashrrev_i32_e32 v77, 31, v76
	v_and_b32_e32 v79, 0xffff0000, v127
	v_lshlrev_b32_e32 v80, 16, v122
	v_and_b32_e32 v81, 0xffff0000, v122
	v_lshlrev_b32_e32 v82, 16, v123
	v_and_b32_e32 v83, 0xffff0000, v123
	v_lshlrev_b32_e32 v84, 16, v118
	v_and_b32_e32 v85, 0xffff0000, v118
	v_lshlrev_b32_e32 v86, 16, v119
	v_and_b32_e32 v87, 0xffff0000, v119
	v_lshlrev_b32_e32 v88, 16, v114
	v_and_b32_e32 v89, 0xffff0000, v114
	v_lshlrev_b32_e32 v90, 16, v115
	v_and_b32_e32 v91, 0xffff0000, v115
	v_lshlrev_b32_e32 v92, 16, v110
	v_and_b32_e32 v93, 0xffff0000, v110
	v_lshlrev_b32_e32 v94, 16, v111
	v_and_b32_e32 v95, 0xffff0000, v111
	v_lshlrev_b32_e32 v98, 16, v106
	v_and_b32_e32 v99, 0xffff0000, v106
	s_mul_i32 s13, s13, 0x8900
	v_mov_b32_e32 v164, v71
	v_bfe_u32 v71, v210, 4, 7
	v_lshlrev_b64 v[72:73], 16, v[76:77]
	v_lshl_add_u64 v[72:73], s[4:5], 0, v[72:73]
	v_lshlrev_b32_e32 v74, 8, v71
	v_mov_b32_e32 v75, v3
	v_lshl_add_u64 v[72:73], v[72:73], 0, v[74:75]
	v_lshl_add_u64 v[72:73], v[72:73], 0, v[194:195]
	global_load_dwordx4 v[136:139], v[72:73], off
	v_mad_i32_i24 v76, v76, s6, v70
	v_mul_u32_u24_e32 v71, 0x110, v71
	v_add3_u32 v71, v76, v71, v194
	v_mov_b32_e32 v165, v71
	v_add_u32_e32 v71, 0x400, v209
	v_ashrrev_i32_e32 v76, 11, v71
	v_ashrrev_i32_e32 v77, 31, v76
	v_bfe_u32 v71, v71, 4, 7
	v_lshlrev_b64 v[72:73], 16, v[76:77]
	v_lshl_add_u64 v[72:73], s[4:5], 0, v[72:73]
	v_lshlrev_b32_e32 v74, 8, v71
	v_mov_b32_e32 v75, v3
	v_lshl_add_u64 v[72:73], v[72:73], 0, v[74:75]
	v_lshl_add_u64 v[72:73], v[72:73], 0, v[194:195]
	global_load_dwordx4 v[140:143], v[72:73], off
	v_mad_i32_i24 v76, v76, s6, v70
	v_mul_u32_u24_e32 v71, 0x110, v71
	v_add3_u32 v71, v76, v71, v194
	v_mov_b32_e32 v166, v71
	v_add_u32_e32 v71, 0x600, v209
	v_ashrrev_i32_e32 v76, 11, v71
	v_ashrrev_i32_e32 v77, 31, v76
	v_bfe_u32 v71, v71, 4, 7
	v_lshlrev_b64 v[72:73], 16, v[76:77]
	v_lshl_add_u64 v[72:73], s[4:5], 0, v[72:73]
	v_lshlrev_b32_e32 v74, 8, v71
	v_mov_b32_e32 v75, v3
	v_lshl_add_u64 v[72:73], v[72:73], 0, v[74:75]
	v_lshl_add_u64 v[72:73], v[72:73], 0, v[194:195]
	global_load_dwordx4 v[144:147], v[72:73], off
	v_mad_i32_i24 v76, v76, s6, v70
	v_mul_u32_u24_e32 v71, 0x110, v71
	v_add3_u32 v71, v76, v71, v194
	v_mov_b32_e32 v167, v71
	v_add_u32_e32 v71, 0x800, v209
	v_ashrrev_i32_e32 v76, 11, v71
	v_ashrrev_i32_e32 v77, 31, v76
	v_lshlrev_b64 v[72:73], 16, v[76:77]
	v_lshl_add_u64 v[72:73], s[4:5], 0, v[72:73]
	v_lshl_add_u64 v[68:69], v[72:73], 0, v[68:69]
	v_lshl_add_u64 v[68:69], v[68:69], 0, v[194:195]
	global_load_dwordx4 v[148:151], v[68:69], off
	v_mad_i32_i24 v68, v76, s6, v70
	v_add3_u32 v68, v68, v78, v194
	v_add_u32_e32 v69, 0xa00, v209
	v_bfe_u32 v71, v69, 4, 7
	v_lshlrev_b32_e32 v76, 16, v126
	v_and_b32_e32 v77, 0xffff0000, v126
	v_lshlrev_b32_e32 v78, 16, v127
	v_mov_b32_e32 v168, v68
	v_ashrrev_i32_e32 v68, 11, v69
	v_ashrrev_i32_e32 v69, 31, v68
	v_lshlrev_b64 v[72:73], 16, v[68:69]
	v_lshl_add_u64 v[72:73], s[4:5], 0, v[72:73]
	v_lshlrev_b32_e32 v74, 8, v71
	v_mov_b32_e32 v75, v3
	v_lshl_add_u64 v[72:73], v[72:73], 0, v[74:75]
	v_lshl_add_u64 v[72:73], v[72:73], 0, v[194:195]
	global_load_dwordx4 v[152:155], v[72:73], off
	v_mad_i32_i24 v68, v68, s6, v70
	v_mul_u32_u24_e32 v69, 0x110, v71
	v_add3_u32 v68, v68, v69, v194
	v_add_u32_e32 v69, 0xc00, v209
	v_bfe_u32 v71, v69, 4, 7
	v_mov_b32_e32 v169, v68
	v_ashrrev_i32_e32 v68, 11, v69
	v_ashrrev_i32_e32 v69, 31, v68
	v_lshlrev_b64 v[72:73], 16, v[68:69]
	v_lshl_add_u64 v[72:73], s[4:5], 0, v[72:73]
	v_lshlrev_b32_e32 v74, 8, v71
	v_mov_b32_e32 v75, v3
	v_lshl_add_u64 v[72:73], v[72:73], 0, v[74:75]
	v_lshl_add_u64 v[72:73], v[72:73], 0, v[194:195]
	global_load_dwordx4 v[156:159], v[72:73], off
	v_mad_i32_i24 v68, v68, s6, v70
	v_mul_u32_u24_e32 v69, 0x110, v71
	v_add3_u32 v68, v68, v69, v194
	v_add_u32_e32 v69, 0xe00, v209
	v_bfe_u32 v71, v69, 4, 7
	v_mov_b32_e32 v170, v68
	v_ashrrev_i32_e32 v68, 11, v69
	v_ashrrev_i32_e32 v69, 31, v68
	v_lshlrev_b64 v[72:73], 16, v[68:69]
	v_lshl_add_u64 v[72:73], s[4:5], 0, v[72:73]
	v_lshlrev_b32_e32 v74, 8, v71
	v_mov_b32_e32 v75, v3
	v_lshl_add_u64 v[72:73], v[72:73], 0, v[74:75]
	v_lshl_add_u64 v[72:73], v[72:73], 0, v[194:195]
	global_load_dwordx4 v[160:163], v[72:73], off
	v_mad_i32_i24 v68, v68, s6, v70
	v_mul_u32_u24_e32 v69, 0x110, v71
	v_add3_u32 v68, v68, v69, v194
	s_mov_b32 s4, 0xc2fc0000
	v_lshlrev_b32_e32 v70, 16, v129
	v_and_b32_e32 v71, 0xffff0000, v129
	v_mov_b32_e32 v171, v68
	s_waitcnt vmcnt(7)
	ds_write_b128 v164, v[132:135]
	s_waitcnt vmcnt(6)
	ds_write_b128 v165, v[136:139]
	s_waitcnt vmcnt(5)
	ds_write_b128 v166, v[140:143]
	s_waitcnt vmcnt(4)
	ds_write_b128 v167, v[144:147]
	s_waitcnt vmcnt(3)
	ds_write_b128 v168, v[148:151]
	s_waitcnt vmcnt(2)
	ds_write_b128 v169, v[152:155]
	s_waitcnt vmcnt(1)
	ds_write_b128 v170, v[156:159]
	s_waitcnt vmcnt(0)
	ds_write_b128 v171, v[160:163]
	v_and_b32_e32 v68, 0x7f, v207
	v_add_u32_e32 v68, 1, v68
	v_cvt_f32_ubyte0_e32 v68, v68
	v_mul_f32_e32 v69, v208, v68
	v_cmp_gt_f32_e32 vcc, s4, v69
	v_mov_b32_e32 v69, 0x42800000
	v_lshlrev_b32_e32 v72, 16, v130
	v_cndmask_b32_e32 v69, 0, v69, vcc
	v_fmac_f32_e32 v69, v208, v68
	v_exp_f32_e32 v68, v69
	v_not_b32_e32 v69, 63
	v_cndmask_b32_e32 v69, 0, v69, vcc
	v_and_b32_e32 v73, 0xffff0000, v130
	v_ldexp_f32 v96, v68, v69
	v_lshlrev_b32_e32 v68, 16, v128
	v_and_b32_e32 v69, 0xffff0000, v128
	v_lshlrev_b32_e32 v74, 16, v131
	v_and_b32_e32 v75, 0xffff0000, v131
	v_pk_mul_f32 v[68:69], v[96:97], v[68:69] op_sel_hi:[0,1]
	v_pk_mul_f32 v[70:71], v[96:97], v[70:71] op_sel_hi:[0,1]
	v_pk_mul_f32 v[72:73], v[96:97], v[72:73] op_sel_hi:[0,1]
	v_pk_mul_f32 v[74:75], v[96:97], v[74:75] op_sel_hi:[0,1]
	v_cvt_pk_bf16_f32 v68, v68, v69
	v_cvt_pk_bf16_f32 v69, v70, v71
	v_cvt_pk_bf16_f32 v70, v72, v73
	v_cvt_pk_bf16_f32 v71, v74, v75
	v_lshlrev_b32_e32 v72, 16, v124
	v_and_b32_e32 v73, 0xffff0000, v124
	v_lshlrev_b32_e32 v74, 16, v125
	v_and_b32_e32 v75, 0xffff0000, v125
	v_pk_mul_f32 v[72:73], v[96:97], v[72:73] op_sel_hi:[0,1]
	v_pk_mul_f32 v[74:75], v[96:97], v[74:75] op_sel_hi:[0,1]
	v_pk_mul_f32 v[76:77], v[96:97], v[76:77] op_sel_hi:[0,1]
	v_pk_mul_f32 v[78:79], v[96:97], v[78:79] op_sel_hi:[0,1]
	v_cvt_pk_bf16_f32 v72, v72, v73
	v_cvt_pk_bf16_f32 v73, v74, v75
	v_cvt_pk_bf16_f32 v74, v76, v77
	v_cvt_pk_bf16_f32 v75, v78, v79
	v_lshlrev_b32_e32 v76, 16, v120
	v_and_b32_e32 v77, 0xffff0000, v120
	v_lshlrev_b32_e32 v78, 16, v121
	v_and_b32_e32 v79, 0xffff0000, v121
	v_pk_mul_f32 v[76:77], v[96:97], v[76:77] op_sel_hi:[0,1]
	v_pk_mul_f32 v[78:79], v[96:97], v[78:79] op_sel_hi:[0,1]
	v_pk_mul_f32 v[80:81], v[96:97], v[80:81] op_sel_hi:[0,1]
	v_pk_mul_f32 v[82:83], v[96:97], v[82:83] op_sel_hi:[0,1]
	v_cvt_pk_bf16_f32 v76, v76, v77
	v_cvt_pk_bf16_f32 v77, v78, v79
	v_cvt_pk_bf16_f32 v78, v80, v81
	v_cvt_pk_bf16_f32 v79, v82, v83
	v_lshlrev_b32_e32 v80, 16, v116
	v_and_b32_e32 v81, 0xffff0000, v116
	v_lshlrev_b32_e32 v82, 16, v117
	v_and_b32_e32 v83, 0xffff0000, v117
	v_pk_mul_f32 v[80:81], v[96:97], v[80:81] op_sel_hi:[0,1]
	v_pk_mul_f32 v[82:83], v[96:97], v[82:83] op_sel_hi:[0,1]
	v_pk_mul_f32 v[84:85], v[96:97], v[84:85] op_sel_hi:[0,1]
	v_pk_mul_f32 v[86:87], v[96:97], v[86:87] op_sel_hi:[0,1]
	v_cvt_pk_bf16_f32 v80, v80, v81
	v_cvt_pk_bf16_f32 v81, v82, v83
	v_cvt_pk_bf16_f32 v82, v84, v85
	v_cvt_pk_bf16_f32 v83, v86, v87
	v_lshlrev_b32_e32 v84, 16, v112
	v_and_b32_e32 v85, 0xffff0000, v112
	v_lshlrev_b32_e32 v86, 16, v113
	v_and_b32_e32 v87, 0xffff0000, v113
	v_pk_mul_f32 v[84:85], v[96:97], v[84:85] op_sel_hi:[0,1]
	v_pk_mul_f32 v[86:87], v[96:97], v[86:87] op_sel_hi:[0,1]
	v_pk_mul_f32 v[88:89], v[96:97], v[88:89] op_sel_hi:[0,1]
	v_pk_mul_f32 v[90:91], v[96:97], v[90:91] op_sel_hi:[0,1]
	v_cvt_pk_bf16_f32 v84, v84, v85
	v_cvt_pk_bf16_f32 v85, v86, v87
	v_cvt_pk_bf16_f32 v86, v88, v89
	v_cvt_pk_bf16_f32 v87, v90, v91
	v_lshlrev_b32_e32 v88, 16, v108
	v_and_b32_e32 v89, 0xffff0000, v108
	v_lshlrev_b32_e32 v90, 16, v109
	v_and_b32_e32 v91, 0xffff0000, v109
	v_pk_mul_f32 v[88:89], v[96:97], v[88:89] op_sel_hi:[0,1]
	v_pk_mul_f32 v[90:91], v[96:97], v[90:91] op_sel_hi:[0,1]
	v_pk_mul_f32 v[92:93], v[96:97], v[92:93] op_sel_hi:[0,1]
	v_pk_mul_f32 v[94:95], v[96:97], v[94:95] op_sel_hi:[0,1]
	v_cvt_pk_bf16_f32 v88, v88, v89
	v_cvt_pk_bf16_f32 v89, v90, v91
	v_cvt_pk_bf16_f32 v90, v92, v93
	v_cvt_pk_bf16_f32 v91, v94, v95
	v_lshlrev_b32_e32 v92, 16, v104
	v_and_b32_e32 v93, 0xffff0000, v104
	v_lshlrev_b32_e32 v94, 16, v105
	v_and_b32_e32 v95, 0xffff0000, v105
	v_lshlrev_b32_e32 v104, 16, v107
	v_and_b32_e32 v105, 0xffff0000, v107
	v_pk_mul_f32 v[92:93], v[96:97], v[92:93] op_sel_hi:[0,1]
	v_pk_mul_f32 v[94:95], v[96:97], v[94:95] op_sel_hi:[0,1]
	v_pk_mul_f32 v[98:99], v[96:97], v[98:99] op_sel_hi:[0,1]
	v_pk_mul_f32 v[104:105], v[96:97], v[104:105] op_sel_hi:[0,1]
	v_cvt_pk_bf16_f32 v92, v92, v93
	v_cvt_pk_bf16_f32 v93, v94, v95
	v_cvt_pk_bf16_f32 v94, v98, v99
	v_cvt_pk_bf16_f32 v95, v104, v105
	v_lshlrev_b32_e32 v98, 16, v100
	v_and_b32_e32 v99, 0xffff0000, v100
	v_lshlrev_b32_e32 v100, 16, v101
	v_and_b32_e32 v101, 0xffff0000, v101
	v_lshlrev_b32_e32 v104, 16, v102
	v_and_b32_e32 v105, 0xffff0000, v102
	v_lshlrev_b32_e32 v102, 16, v103
	v_and_b32_e32 v103, 0xffff0000, v103
	s_add_i32 s4, s72, s13
	v_pk_mul_f32 v[98:99], v[96:97], v[98:99] op_sel_hi:[0,1]
	v_pk_mul_f32 v[100:101], v[96:97], v[100:101] op_sel_hi:[0,1]
	v_pk_mul_f32 v[104:105], v[96:97], v[104:105] op_sel_hi:[0,1]
	v_pk_mul_f32 v[102:103], v[96:97], v[102:103] op_sel_hi:[0,1]
	v_add3_u32 v1, s4, v1, v2
	v_cvt_pk_bf16_f32 v96, v98, v99
	v_cvt_pk_bf16_f32 v97, v100, v101
	v_cvt_pk_bf16_f32 v98, v104, v105
	v_cvt_pk_bf16_f32 v99, v102, v103
	s_waitcnt lgkmcnt(0)
	s_barrier
	ds_read_b128 v[100:103], v1
	ds_read_b128 v[104:107], v1 offset:32
	ds_read_b128 v[108:111], v1 offset:64
	ds_read_b128 v[112:115], v1 offset:96
	ds_read_b128 v[116:119], v1 offset:128
	ds_read_b128 v[120:123], v1 offset:160
	ds_read_b128 v[124:127], v1 offset:192
	ds_read_b128 v[128:131], v1 offset:224
	s_waitcnt lgkmcnt(7)
	v_mfma_f32_32x32x16_bf16 v[52:67], v[100:103], v[68:71], v[52:67]
	s_waitcnt lgkmcnt(6)
	v_mfma_f32_32x32x16_bf16 v[52:67], v[104:107], v[72:75], v[52:67]
	s_waitcnt lgkmcnt(5)
	v_mfma_f32_32x32x16_bf16 v[52:67], v[108:111], v[76:79], v[52:67]
	s_waitcnt lgkmcnt(4)
	v_mfma_f32_32x32x16_bf16 v[52:67], v[112:115], v[80:83], v[52:67]
	s_waitcnt lgkmcnt(3)
	v_mfma_f32_32x32x16_bf16 v[52:67], v[116:119], v[84:87], v[52:67]
	s_waitcnt lgkmcnt(2)
	v_mfma_f32_32x32x16_bf16 v[52:67], v[120:123], v[88:91], v[52:67]
	s_waitcnt lgkmcnt(1)
	v_mfma_f32_32x32x16_bf16 v[52:67], v[124:127], v[92:95], v[52:67]
	s_waitcnt lgkmcnt(0)
	v_mfma_f32_32x32x16_bf16 v[52:67], v[128:131], v[96:99], v[52:67]
	ds_read_b128 v[100:103], v1 offset:8704
	ds_read_b128 v[104:107], v1 offset:8736
	ds_read_b128 v[108:111], v1 offset:8768
	ds_read_b128 v[112:115], v1 offset:8800
	ds_read_b128 v[116:119], v1 offset:8832
	ds_read_b128 v[120:123], v1 offset:8864
	ds_read_b128 v[124:127], v1 offset:8896
	ds_read_b128 v[128:131], v1 offset:8928
	s_waitcnt lgkmcnt(7)
	v_mfma_f32_32x32x16_bf16 v[36:51], v[100:103], v[68:71], v[36:51]
	s_waitcnt lgkmcnt(6)
	v_mfma_f32_32x32x16_bf16 v[36:51], v[104:107], v[72:75], v[36:51]
	s_waitcnt lgkmcnt(5)
	v_mfma_f32_32x32x16_bf16 v[36:51], v[108:111], v[76:79], v[36:51]
	s_waitcnt lgkmcnt(4)
	v_mfma_f32_32x32x16_bf16 v[36:51], v[112:115], v[80:83], v[36:51]
	s_waitcnt lgkmcnt(3)
	v_mfma_f32_32x32x16_bf16 v[36:51], v[116:119], v[84:87], v[36:51]
	s_waitcnt lgkmcnt(2)
	v_mfma_f32_32x32x16_bf16 v[36:51], v[120:123], v[88:91], v[36:51]
	s_waitcnt lgkmcnt(1)
	v_mfma_f32_32x32x16_bf16 v[36:51], v[124:127], v[92:95], v[36:51]
	s_waitcnt lgkmcnt(0)
	v_mfma_f32_32x32x16_bf16 v[36:51], v[128:131], v[96:99], v[36:51]
	ds_read_b128 v[100:103], v1 offset:17408
	ds_read_b128 v[104:107], v1 offset:17440
	ds_read_b128 v[108:111], v1 offset:17472
	ds_read_b128 v[112:115], v1 offset:17504
	ds_read_b128 v[116:119], v1 offset:17536
	ds_read_b128 v[120:123], v1 offset:17568
	ds_read_b128 v[124:127], v1 offset:17600
	ds_read_b128 v[128:131], v1 offset:17632
	s_waitcnt lgkmcnt(7)
	v_mfma_f32_32x32x16_bf16 v[20:35], v[100:103], v[68:71], v[20:35]
	s_waitcnt lgkmcnt(6)
	v_mfma_f32_32x32x16_bf16 v[20:35], v[104:107], v[72:75], v[20:35]
	s_waitcnt lgkmcnt(5)
	v_mfma_f32_32x32x16_bf16 v[20:35], v[108:111], v[76:79], v[20:35]
	s_waitcnt lgkmcnt(4)
	v_mfma_f32_32x32x16_bf16 v[20:35], v[112:115], v[80:83], v[20:35]
	s_waitcnt lgkmcnt(3)
	v_mfma_f32_32x32x16_bf16 v[20:35], v[116:119], v[84:87], v[20:35]
	s_waitcnt lgkmcnt(2)
	v_mfma_f32_32x32x16_bf16 v[20:35], v[120:123], v[88:91], v[20:35]
	s_waitcnt lgkmcnt(1)
	v_mfma_f32_32x32x16_bf16 v[20:35], v[124:127], v[92:95], v[20:35]
	s_waitcnt lgkmcnt(0)
	v_mfma_f32_32x32x16_bf16 v[20:35], v[128:131], v[96:99], v[20:35]
	ds_read_b128 v[100:103], v1 offset:26112
	ds_read_b128 v[104:107], v1 offset:26144
	ds_read_b128 v[108:111], v1 offset:26176
	ds_read_b128 v[112:115], v1 offset:26208
	ds_read_b128 v[116:119], v1 offset:26240
	ds_read_b128 v[120:123], v1 offset:26272
	ds_read_b128 v[124:127], v1 offset:26304
	ds_read_b128 v[128:131], v1 offset:26336
	s_waitcnt lgkmcnt(7)
	v_mfma_f32_32x32x16_bf16 v[4:19], v[100:103], v[68:71], v[4:19]
	s_waitcnt lgkmcnt(6)
	v_mfma_f32_32x32x16_bf16 v[4:19], v[104:107], v[72:75], v[4:19]
	s_waitcnt lgkmcnt(5)
	v_mfma_f32_32x32x16_bf16 v[4:19], v[108:111], v[76:79], v[4:19]
	s_waitcnt lgkmcnt(4)
	v_mfma_f32_32x32x16_bf16 v[4:19], v[112:115], v[80:83], v[4:19]
	s_waitcnt lgkmcnt(3)
	v_mfma_f32_32x32x16_bf16 v[4:19], v[116:119], v[84:87], v[4:19]
	s_waitcnt lgkmcnt(2)
	v_mfma_f32_32x32x16_bf16 v[4:19], v[120:123], v[88:91], v[4:19]
	s_waitcnt lgkmcnt(1)
	v_mfma_f32_32x32x16_bf16 v[4:19], v[124:127], v[92:95], v[4:19]
	s_waitcnt lgkmcnt(0)
	v_mfma_f32_32x32x16_bf16 v[4:19], v[128:131], v[96:99], v[4:19]
	v_add_f32_e32 v1, 0, v52
	v_add_f32_e32 v1, v53, v1
	v_add_f32_e32 v1, v54, v1
	v_add_f32_e32 v1, v55, v1
	v_add_f32_e32 v1, v56, v1
	v_add_f32_e32 v1, v57, v1
	v_add_f32_e32 v1, v58, v1
	v_add_f32_e32 v1, v59, v1
	v_add_f32_e32 v1, v60, v1
	v_add_f32_e32 v1, v61, v1
	v_add_f32_e32 v1, v62, v1
	v_add_f32_e32 v1, v63, v1
	v_add_f32_e32 v1, v64, v1
	v_add_f32_e32 v1, v65, v1
	v_add_f32_e32 v1, v66, v1
	v_add_f32_e32 v1, v67, v1
	v_add_f32_e32 v1, v1, v36
	v_add_f32_e32 v1, v37, v1
	v_add_f32_e32 v1, v38, v1
	v_add_f32_e32 v1, v39, v1
	v_add_f32_e32 v1, v40, v1
	v_add_f32_e32 v1, v41, v1
	v_add_f32_e32 v1, v42, v1
	v_add_f32_e32 v1, v43, v1
	v_add_f32_e32 v1, v44, v1
	v_add_f32_e32 v1, v45, v1
	v_add_f32_e32 v1, v46, v1
	v_add_f32_e32 v1, v47, v1
	v_add_f32_e32 v1, v48, v1
	v_add_f32_e32 v1, v49, v1
	v_add_f32_e32 v1, v50, v1
	v_add_f32_e32 v1, v51, v1
	v_add_f32_e32 v1, v1, v20
	v_add_f32_e32 v1, v21, v1
	v_add_f32_e32 v1, v22, v1
	v_add_f32_e32 v1, v23, v1
	v_add_f32_e32 v1, v24, v1
	v_add_f32_e32 v1, v25, v1
	v_add_f32_e32 v1, v26, v1
	v_add_f32_e32 v1, v27, v1
	v_add_f32_e32 v1, v28, v1
	v_add_f32_e32 v1, v29, v1
	v_add_f32_e32 v1, v30, v1
	v_add_f32_e32 v1, v31, v1
	v_add_f32_e32 v1, v32, v1
	v_add_f32_e32 v1, v33, v1
	v_add_f32_e32 v1, v34, v1
	v_add_f32_e32 v1, v35, v1
	v_add_f32_e32 v1, v1, v4
	v_add_f32_e32 v1, v5, v1
	v_add_f32_e32 v1, v6, v1
	v_add_f32_e32 v1, v7, v1
	v_add_f32_e32 v1, v8, v1
	v_add_f32_e32 v1, v9, v1
	v_add_f32_e32 v1, v10, v1
	v_add_f32_e32 v1, v11, v1
	v_add_f32_e32 v1, v12, v1
	v_add_f32_e32 v1, v13, v1
	v_add_f32_e32 v1, v14, v1
	v_add_f32_e32 v1, v15, v1
	v_add_f32_e32 v1, v16, v1
	v_add_f32_e32 v1, v17, v1
	v_add_f32_e32 v1, v18, v1
	v_add_f32_e32 v2, v19, v1
	v_xor_b32_e32 v1, 32, v230
	v_cmp_lt_i32_e32 vcc, v1, v231
	v_lshlrev_b64 v[68:69], 12, v[180:181]
	v_readlane_b32 s4, v253, 17
	v_cndmask_b32_e32 v1, v230, v1, vcc
	v_lshlrev_b32_e32 v1, 2, v1
	ds_bpermute_b32 v70, v1, v2
	v_lshl_add_u64 v[68:69], s[2:3], 0, v[68:69]
	v_readlane_b32 s5, v253, 18
	s_movk_i32 s20, 0x110
	v_readlane_b32 s6, v253, 19
	s_waitcnt lgkmcnt(0)
	v_add_f32_e32 v2, v2, v70
	v_mul_f32_e32 v78, 0x3c000000, v2
	v_pk_add_f32 v[70:71], v[14:15], v[78:79] op_sel_hi:[1,0] neg_lo:[0,1] neg_hi:[0,1]
	v_pk_add_f32 v[14:15], v[18:19], v[78:79] op_sel_hi:[1,0] neg_lo:[0,1] neg_hi:[0,1]
	v_lshl_add_u64 v[18:19], v[68:69], 0, s[4:5]
	v_mov_b64_e32 v[68:69], s[2:3]
	v_mad_i64_i32 v[68:69], s[2:3], v180, s24, v[68:69]
	v_lshl_add_u64 v[68:69], v[68:69], 0, s[4:5]
	v_lshlrev_b32_e32 v2, 1, v206
	v_lshl_add_u64 v[80:81], v[68:69], 0, v[2:3]
	s_mov_b64 s[2:3], 0x9000c00
	v_lshl_add_u64 v[68:69], v[80:81], 0, s[2:3]
	s_mov_b32 s2, 0x9000000
	v_add_co_u32_e32 v80, vcc, s2, v80
	global_load_dwordx2 v[92:93], v[68:69], off offset:16
	global_load_dwordx2 v[100:101], v[68:69], off offset:32
	global_load_dwordx2 v[104:105], v[68:69], off offset:48
	global_load_dwordx2 v[108:109], v[68:69], off offset:64
	v_addc_co_u32_e32 v81, vcc, 0, v81, vcc
	global_load_dwordx2 v[82:83], v[80:81], off offset:3072
	v_pk_add_f32 v[16:17], v[16:17], v[78:79] op_sel_hi:[1,0] neg_lo:[0,1] neg_hi:[0,1]
	v_pk_add_f32 v[54:55], v[54:55], v[78:79] op_sel_hi:[1,0] neg_lo:[0,1] neg_hi:[0,1]
	v_pk_add_f32 v[52:53], v[52:53], v[78:79] op_sel_hi:[1,0] neg_lo:[0,1] neg_hi:[0,1]
	global_load_dwordx2 v[114:115], v[68:69], off offset:80
	global_load_dwordx2 v[120:121], v[68:69], off offset:96
	global_load_dwordx2 v[128:129], v[68:69], off offset:112
	global_load_dwordx2 v[136:137], v[68:69], off offset:128
	global_load_dwordx2 v[144:145], v[68:69], off offset:144
	global_load_dwordx2 v[152:153], v[68:69], off offset:160
	global_load_dwordx2 v[160:161], v[68:69], off offset:176
	global_load_dwordx2 v[166:167], v[68:69], off offset:192
	v_pk_mul_f32 v[88:89], v[52:53], v[52:53]
	v_pk_mul_f32 v[86:87], v[54:55], v[54:55]
	v_pk_mul_f32 v[72:73], v[70:71], v[70:71]
	v_pk_mul_f32 v[74:75], v[16:17], v[16:17]
	v_pk_mul_f32 v[76:77], v[14:15], v[14:15]
	s_mov_b64 s[2:3], 0x25800000
	v_readlane_b32 s7, v253, 20
	s_waitcnt vmcnt(0) lgkmcnt(0)
	v_lshlrev_b32_e32 v90, 16, v92
	v_and_b32_e32 v91, 0xffff0000, v92
	v_lshlrev_b32_e32 v92, 16, v93
	v_and_b32_e32 v93, 0xffff0000, v93
	v_lshlrev_b32_e32 v80, 16, v82
	v_mul_f32_e32 v79, 0xbfb8aa3b, v80
	v_exp_f32_e32 v79, v79
	v_and_b32_e32 v81, 0xffff0000, v82
	v_lshlrev_b32_e32 v82, 16, v83
	v_and_b32_e32 v83, 0xffff0000, v83
	v_add_f32_e32 v79, 1.0, v79
	v_rcp_f32_e32 v84, v79
	v_mul_f32_e32 v79, 0xbfb8aa3b, v81
	v_exp_f32_e32 v79, v79
	s_nop 0
	v_add_f32_e32 v79, 1.0, v79
	v_rcp_f32_e32 v85, v79
	v_mul_f32_e32 v79, 0xbfb8aa3b, v82
	v_exp_f32_e32 v79, v79
	v_pk_mul_f32 v[80:81], v[84:85], v[80:81]
	v_add_f32_e32 v79, 1.0, v79
	v_rcp_f32_e32 v84, v79
	v_mul_f32_e32 v79, 0xbfb8aa3b, v83
	v_exp_f32_e32 v79, v79
	s_nop 0
	v_add_f32_e32 v79, 1.0, v79
	v_rcp_f32_e32 v85, v79
	v_pk_add_f32 v[56:57], v[56:57], v[78:79] op_sel_hi:[1,0] neg_lo:[0,1] neg_hi:[0,1]
	v_pk_add_f32 v[58:59], v[58:59], v[78:79] op_sel_hi:[1,0] neg_lo:[0,1] neg_hi:[0,1]
	v_pk_mul_f32 v[96:97], v[56:57], v[56:57]
	v_pk_mul_f32 v[84:85], v[84:85], v[82:83]
	v_lshl_add_u64 v[82:83], v[18:19], 0, v[2:3]
	v_mul_f32_e32 v2, 0xbfb8aa3b, v90
	v_exp_f32_e32 v2, v2
	v_pk_mul_f32 v[94:95], v[58:59], v[58:59]
	v_pk_add_f32 v[60:61], v[60:61], v[78:79] op_sel_hi:[1,0] neg_lo:[0,1] neg_hi:[0,1]
	v_pk_add_f32 v[62:63], v[62:63], v[78:79] op_sel_hi:[1,0] neg_lo:[0,1] neg_hi:[0,1]
	v_add_f32_e32 v2, 1.0, v2
	v_rcp_f32_e32 v98, v2
	v_mul_f32_e32 v2, 0xbfb8aa3b, v91
	v_exp_f32_e32 v2, v2
	v_pk_mul_f32 v[116:117], v[60:61], v[60:61]
	v_pk_mul_f32 v[112:113], v[62:63], v[62:63]
	v_pk_add_f32 v[64:65], v[64:65], v[78:79] op_sel_hi:[1,0] neg_lo:[0,1] neg_hi:[0,1]
	v_add_f32_e32 v2, 1.0, v2
	v_rcp_f32_e32 v99, v2
	v_mul_f32_e32 v2, 0xbfb8aa3b, v92
	v_exp_f32_e32 v2, v2
	v_pk_mul_f32 v[124:125], v[64:65], v[64:65]
	v_pk_mul_f32 v[90:91], v[98:99], v[90:91]
	v_pk_add_f32 v[66:67], v[66:67], v[78:79] op_sel_hi:[1,0] neg_lo:[0,1] neg_hi:[0,1]
	v_add_f32_e32 v2, 1.0, v2
	v_rcp_f32_e32 v98, v2
	v_mul_f32_e32 v2, 0xbfb8aa3b, v93
	v_exp_f32_e32 v2, v2
	v_pk_mul_f32 v[122:123], v[66:67], v[66:67]
	v_pk_add_f32 v[36:37], v[36:37], v[78:79] op_sel_hi:[1,0] neg_lo:[0,1] neg_hi:[0,1]
	v_pk_add_f32 v[38:39], v[38:39], v[78:79] op_sel_hi:[1,0] neg_lo:[0,1] neg_hi:[0,1]
	v_add_f32_e32 v2, 1.0, v2
	v_rcp_f32_e32 v99, v2
	v_pk_mul_f32 v[132:133], v[36:37], v[36:37]
	v_pk_mul_f32 v[130:131], v[38:39], v[38:39]
	v_pk_add_f32 v[40:41], v[40:41], v[78:79] op_sel_hi:[1,0] neg_lo:[0,1] neg_hi:[0,1]
	v_pk_mul_f32 v[92:93], v[98:99], v[92:93]
	v_lshlrev_b32_e32 v98, 16, v100
	v_mul_f32_e32 v2, 0xbfb8aa3b, v98
	v_exp_f32_e32 v2, v2
	v_and_b32_e32 v99, 0xffff0000, v100
	v_lshlrev_b32_e32 v100, 16, v101
	v_and_b32_e32 v101, 0xffff0000, v101
	v_add_f32_e32 v2, 1.0, v2
	v_rcp_f32_e32 v102, v2
	v_mul_f32_e32 v2, 0xbfb8aa3b, v99
	v_exp_f32_e32 v2, v2
	v_pk_mul_f32 v[140:141], v[40:41], v[40:41]
	v_pk_add_f32 v[42:43], v[42:43], v[78:79] op_sel_hi:[1,0] neg_lo:[0,1] neg_hi:[0,1]
	v_pk_add_f32 v[44:45], v[44:45], v[78:79] op_sel_hi:[1,0] neg_lo:[0,1] neg_hi:[0,1]
	v_add_f32_e32 v2, 1.0, v2
	v_rcp_f32_e32 v103, v2
	v_mul_f32_e32 v2, 0xbfb8aa3b, v100
	v_exp_f32_e32 v2, v2
	v_pk_mul_f32 v[138:139], v[42:43], v[42:43]
	v_pk_mul_f32 v[98:99], v[102:103], v[98:99]
	v_pk_mul_f32 v[150:151], v[44:45], v[44:45]
	v_add_f32_e32 v2, 1.0, v2
	v_rcp_f32_e32 v102, v2
	v_mul_f32_e32 v2, 0xbfb8aa3b, v101
	v_exp_f32_e32 v2, v2
	v_pk_add_f32 v[46:47], v[46:47], v[78:79] op_sel_hi:[1,0] neg_lo:[0,1] neg_hi:[0,1]
	v_pk_add_f32 v[48:49], v[48:49], v[78:79] op_sel_hi:[1,0] neg_lo:[0,1] neg_hi:[0,1]
	v_pk_mul_f32 v[146:147], v[46:47], v[46:47]
	v_add_f32_e32 v2, 1.0, v2
	v_rcp_f32_e32 v103, v2
	v_pk_mul_f32 v[158:159], v[48:49], v[48:49]
	v_pk_add_f32 v[50:51], v[50:51], v[78:79] op_sel_hi:[1,0] neg_lo:[0,1] neg_hi:[0,1]
	v_pk_add_f32 v[20:21], v[20:21], v[78:79] op_sel_hi:[1,0] neg_lo:[0,1] neg_hi:[0,1]
	v_pk_mul_f32 v[100:101], v[102:103], v[100:101]
	v_lshlrev_b32_e32 v102, 16, v104
	v_mul_f32_e32 v2, 0xbfb8aa3b, v102
	v_exp_f32_e32 v2, v2
	v_and_b32_e32 v103, 0xffff0000, v104
	v_lshlrev_b32_e32 v104, 16, v105
	v_and_b32_e32 v105, 0xffff0000, v105
	v_add_f32_e32 v2, 1.0, v2
	v_rcp_f32_e32 v106, v2
	v_mul_f32_e32 v2, 0xbfb8aa3b, v103
	v_exp_f32_e32 v2, v2
	v_pk_mul_f32 v[156:157], v[50:51], v[50:51]
	v_pk_mul_f32 v[168:169], v[20:21], v[20:21]
	v_pk_add_f32 v[22:23], v[22:23], v[78:79] op_sel_hi:[1,0] neg_lo:[0,1] neg_hi:[0,1]
	v_add_f32_e32 v2, 1.0, v2
	v_rcp_f32_e32 v107, v2
	v_mul_f32_e32 v2, 0xbfb8aa3b, v104
	v_exp_f32_e32 v2, v2
	v_pk_mul_f32 v[164:165], v[22:23], v[22:23]
	v_pk_mul_f32 v[102:103], v[106:107], v[102:103]
	v_pk_add_f32 v[24:25], v[24:25], v[78:79] op_sel_hi:[1,0] neg_lo:[0,1] neg_hi:[0,1]
	v_add_f32_e32 v2, 1.0, v2
	v_rcp_f32_e32 v106, v2
	v_mul_f32_e32 v2, 0xbfb8aa3b, v105
	v_exp_f32_e32 v2, v2
	v_pk_mul_f32 v[172:173], v[24:25], v[24:25]
	v_pk_add_f32 v[26:27], v[26:27], v[78:79] op_sel_hi:[1,0] neg_lo:[0,1] neg_hi:[0,1]
	v_pk_add_f32 v[28:29], v[28:29], v[78:79] op_sel_hi:[1,0] neg_lo:[0,1] neg_hi:[0,1]
	v_add_f32_e32 v2, 1.0, v2
	v_rcp_f32_e32 v107, v2
	v_pk_mul_f32 v[170:171], v[26:27], v[26:27]
	v_pk_mul_f32 v[176:177], v[28:29], v[28:29]
	v_pk_add_f32 v[30:31], v[30:31], v[78:79] op_sel_hi:[1,0] neg_lo:[0,1] neg_hi:[0,1]
	v_pk_mul_f32 v[104:105], v[106:107], v[104:105]
	v_lshlrev_b32_e32 v106, 16, v108
	v_mul_f32_e32 v2, 0xbfb8aa3b, v106
	v_exp_f32_e32 v2, v2
	v_and_b32_e32 v107, 0xffff0000, v108
	v_lshlrev_b32_e32 v108, 16, v109
	v_and_b32_e32 v109, 0xffff0000, v109
	v_add_f32_e32 v2, 1.0, v2
	v_rcp_f32_e32 v110, v2
	v_mul_f32_e32 v2, 0xbfb8aa3b, v107
	v_exp_f32_e32 v2, v2
	v_pk_mul_f32 v[174:175], v[30:31], v[30:31]
	v_pk_add_f32 v[32:33], v[32:33], v[78:79] op_sel_hi:[1,0] neg_lo:[0,1] neg_hi:[0,1]
	v_pk_add_f32 v[34:35], v[34:35], v[78:79] op_sel_hi:[1,0] neg_lo:[0,1] neg_hi:[0,1]
	v_add_f32_e32 v2, 1.0, v2
	v_rcp_f32_e32 v111, v2
	v_mul_f32_e32 v2, 0xbfb8aa3b, v108
	v_exp_f32_e32 v2, v2
	v_pk_mul_f32 v[180:181], v[32:33], v[32:33]
	v_pk_mul_f32 v[106:107], v[110:111], v[106:107]
	v_pk_mul_f32 v[178:179], v[34:35], v[34:35]
	v_add_f32_e32 v2, 1.0, v2
	v_rcp_f32_e32 v110, v2
	v_mul_f32_e32 v2, 0xbfb8aa3b, v109
	v_exp_f32_e32 v2, v2
	v_pk_add_f32 v[4:5], v[4:5], v[78:79] op_sel_hi:[1,0] neg_lo:[0,1] neg_hi:[0,1]
	v_pk_add_f32 v[6:7], v[6:7], v[78:79] op_sel_hi:[1,0] neg_lo:[0,1] neg_hi:[0,1]
	v_pk_mul_f32 v[196:197], v[4:5], v[4:5]
	v_add_f32_e32 v2, 1.0, v2
	v_rcp_f32_e32 v111, v2
	v_pk_mul_f32 v[194:195], v[6:7], v[6:7]
	v_pk_add_f32 v[8:9], v[8:9], v[78:79] op_sel_hi:[1,0] neg_lo:[0,1] neg_hi:[0,1]
	v_pk_add_f32 v[10:11], v[10:11], v[78:79] op_sel_hi:[1,0] neg_lo:[0,1] neg_hi:[0,1]
	v_pk_mul_f32 v[108:109], v[110:111], v[108:109]
	v_lshlrev_b32_e32 v110, 16, v114
	v_mul_f32_e32 v2, 0xbfb8aa3b, v110
	v_exp_f32_e32 v2, v2
	v_and_b32_e32 v111, 0xffff0000, v114
	v_lshlrev_b32_e32 v114, 16, v115
	v_and_b32_e32 v115, 0xffff0000, v115
	v_add_f32_e32 v2, 1.0, v2
	v_rcp_f32_e32 v118, v2
	v_mul_f32_e32 v2, 0xbfb8aa3b, v111
	v_exp_f32_e32 v2, v2
	v_pk_mul_f32 v[186:187], v[8:9], v[8:9]
	v_pk_mul_f32 v[184:185], v[10:11], v[10:11]
	v_pk_add_f32 v[12:13], v[12:13], v[78:79] op_sel_hi:[1,0] neg_lo:[0,1] neg_hi:[0,1]
	v_add_f32_e32 v2, 1.0, v2
	v_rcp_f32_e32 v119, v2
	v_mul_f32_e32 v2, 0xbfb8aa3b, v114
	v_exp_f32_e32 v2, v2
	v_pk_mul_f32 v[78:79], v[12:13], v[12:13]
	v_pk_mul_f32 v[110:111], v[118:119], v[110:111]
	v_lshl_add_u64 v[18:19], v[82:83], 0, s[2:3]
	v_add_f32_e32 v2, 1.0, v2
	v_rcp_f32_e32 v118, v2
	v_mul_f32_e32 v2, 0xbfb8aa3b, v115
	v_exp_f32_e32 v2, v2
	s_mov_b32 s2, 0x25800000
	v_add_f32_e32 v2, 1.0, v2
	v_rcp_f32_e32 v119, v2
	s_nop 0
	v_pk_mul_f32 v[114:115], v[118:119], v[114:115]
	v_lshlrev_b32_e32 v118, 16, v120
	v_mul_f32_e32 v2, 0xbfb8aa3b, v118
	v_exp_f32_e32 v2, v2
	v_and_b32_e32 v119, 0xffff0000, v120
	v_lshlrev_b32_e32 v120, 16, v121
	v_and_b32_e32 v121, 0xffff0000, v121
	v_add_f32_e32 v2, 1.0, v2
	v_rcp_f32_e32 v126, v2
	v_mul_f32_e32 v2, 0xbfb8aa3b, v119
	v_exp_f32_e32 v2, v2
	s_nop 0
	v_add_f32_e32 v2, 1.0, v2
	v_rcp_f32_e32 v127, v2
	v_mul_f32_e32 v2, 0xbfb8aa3b, v120
	v_exp_f32_e32 v2, v2
	v_pk_mul_f32 v[118:119], v[126:127], v[118:119]
	v_add_f32_e32 v2, 1.0, v2
	v_rcp_f32_e32 v126, v2
	v_mul_f32_e32 v2, 0xbfb8aa3b, v121
	v_exp_f32_e32 v2, v2
	s_nop 0
	v_add_f32_e32 v2, 1.0, v2
	v_rcp_f32_e32 v127, v2
	s_nop 0
	v_pk_mul_f32 v[120:121], v[126:127], v[120:121]
	v_lshlrev_b32_e32 v126, 16, v128
	v_mul_f32_e32 v2, 0xbfb8aa3b, v126
	v_exp_f32_e32 v2, v2
	v_and_b32_e32 v127, 0xffff0000, v128
	v_lshlrev_b32_e32 v128, 16, v129
	v_and_b32_e32 v129, 0xffff0000, v129
	v_add_f32_e32 v2, 1.0, v2
	v_rcp_f32_e32 v134, v2
	v_mul_f32_e32 v2, 0xbfb8aa3b, v127
	v_exp_f32_e32 v2, v2
	s_nop 0
	v_add_f32_e32 v2, 1.0, v2
	v_rcp_f32_e32 v135, v2
	v_mul_f32_e32 v2, 0xbfb8aa3b, v128
	v_exp_f32_e32 v2, v2
	v_pk_mul_f32 v[126:127], v[134:135], v[126:127]
	v_add_f32_e32 v2, 1.0, v2
	v_rcp_f32_e32 v134, v2
	v_mul_f32_e32 v2, 0xbfb8aa3b, v129
	v_exp_f32_e32 v2, v2
	s_nop 0
	v_add_f32_e32 v2, 1.0, v2
	v_rcp_f32_e32 v135, v2
	s_nop 0
	v_pk_mul_f32 v[128:129], v[134:135], v[128:129]
	v_lshlrev_b32_e32 v134, 16, v136
	v_mul_f32_e32 v2, 0xbfb8aa3b, v134
	v_exp_f32_e32 v2, v2
	v_and_b32_e32 v135, 0xffff0000, v136
	v_lshlrev_b32_e32 v136, 16, v137
	v_and_b32_e32 v137, 0xffff0000, v137
	v_add_f32_e32 v2, 1.0, v2
	v_rcp_f32_e32 v142, v2
	v_mul_f32_e32 v2, 0xbfb8aa3b, v135
	v_exp_f32_e32 v2, v2
	s_nop 0
	v_add_f32_e32 v2, 1.0, v2
	v_rcp_f32_e32 v143, v2
	v_mul_f32_e32 v2, 0xbfb8aa3b, v136
	v_exp_f32_e32 v2, v2
	v_pk_mul_f32 v[134:135], v[142:143], v[134:135]
	v_add_f32_e32 v2, 1.0, v2
	v_rcp_f32_e32 v142, v2
	v_mul_f32_e32 v2, 0xbfb8aa3b, v137
	v_exp_f32_e32 v2, v2
	s_nop 0
	v_add_f32_e32 v2, 1.0, v2
	v_rcp_f32_e32 v143, v2
	s_nop 0
	v_pk_mul_f32 v[136:137], v[142:143], v[136:137]
	v_lshlrev_b32_e32 v142, 16, v144
	v_mul_f32_e32 v2, 0xbfb8aa3b, v142
	v_exp_f32_e32 v2, v2
	v_and_b32_e32 v143, 0xffff0000, v144
	v_lshlrev_b32_e32 v144, 16, v145
	v_and_b32_e32 v145, 0xffff0000, v145
	v_add_f32_e32 v2, 1.0, v2
	v_rcp_f32_e32 v148, v2
	v_mul_f32_e32 v2, 0xbfb8aa3b, v143
	v_exp_f32_e32 v2, v2
	s_nop 0
	v_add_f32_e32 v2, 1.0, v2
	v_rcp_f32_e32 v149, v2
	v_mul_f32_e32 v2, 0xbfb8aa3b, v144
	v_exp_f32_e32 v2, v2
	v_pk_mul_f32 v[142:143], v[148:149], v[142:143]
	v_add_f32_e32 v2, 1.0, v2
	v_rcp_f32_e32 v148, v2
	v_mul_f32_e32 v2, 0xbfb8aa3b, v145
	v_exp_f32_e32 v2, v2
	s_nop 0
	v_add_f32_e32 v2, 1.0, v2
	v_rcp_f32_e32 v149, v2
	s_nop 0
	v_pk_mul_f32 v[144:145], v[148:149], v[144:145]
	v_lshlrev_b32_e32 v148, 16, v152
	v_mul_f32_e32 v2, 0xbfb8aa3b, v148
	v_exp_f32_e32 v2, v2
	v_and_b32_e32 v149, 0xffff0000, v152
	v_lshlrev_b32_e32 v152, 16, v153
	v_and_b32_e32 v153, 0xffff0000, v153
	v_add_f32_e32 v2, 1.0, v2
	v_rcp_f32_e32 v154, v2
	v_mul_f32_e32 v2, 0xbfb8aa3b, v149
	v_exp_f32_e32 v2, v2
	s_nop 0
	v_add_f32_e32 v2, 1.0, v2
	v_rcp_f32_e32 v155, v2
	v_mul_f32_e32 v2, 0xbfb8aa3b, v152
	v_exp_f32_e32 v2, v2
	v_pk_mul_f32 v[148:149], v[154:155], v[148:149]
	v_add_f32_e32 v2, 1.0, v2
	v_rcp_f32_e32 v154, v2
	v_mul_f32_e32 v2, 0xbfb8aa3b, v153
	v_exp_f32_e32 v2, v2
	s_nop 0
	v_add_f32_e32 v2, 1.0, v2
	v_rcp_f32_e32 v155, v2
	s_nop 0
	v_pk_mul_f32 v[152:153], v[154:155], v[152:153]
	v_lshlrev_b32_e32 v154, 16, v160
	v_mul_f32_e32 v2, 0xbfb8aa3b, v154
	v_exp_f32_e32 v2, v2
	v_and_b32_e32 v155, 0xffff0000, v160
	v_lshlrev_b32_e32 v160, 16, v161
	v_and_b32_e32 v161, 0xffff0000, v161
	v_add_f32_e32 v2, 1.0, v2
	v_rcp_f32_e32 v162, v2
	v_mul_f32_e32 v2, 0xbfb8aa3b, v155
	v_exp_f32_e32 v2, v2
	s_nop 0
	v_add_f32_e32 v2, 1.0, v2
	v_rcp_f32_e32 v163, v2
	v_mul_f32_e32 v2, 0xbfb8aa3b, v160
	v_exp_f32_e32 v2, v2
	v_pk_mul_f32 v[154:155], v[162:163], v[154:155]
	v_add_f32_e32 v2, 1.0, v2
	v_rcp_f32_e32 v162, v2
	v_mul_f32_e32 v2, 0xbfb8aa3b, v161
	v_exp_f32_e32 v2, v2
	s_nop 0
	v_add_f32_e32 v2, 1.0, v2
	v_rcp_f32_e32 v163, v2
	s_nop 0
	v_pk_mul_f32 v[160:161], v[162:163], v[160:161]
	v_lshlrev_b32_e32 v162, 16, v166
	v_mul_f32_e32 v2, 0xbfb8aa3b, v162
	v_exp_f32_e32 v2, v2
	v_and_b32_e32 v163, 0xffff0000, v166
	v_lshlrev_b32_e32 v166, 16, v167
	v_and_b32_e32 v167, 0xffff0000, v167
	v_add_f32_e32 v2, 1.0, v2
	v_rcp_f32_e32 v182, v2
	v_mul_f32_e32 v2, 0xbfb8aa3b, v163
	v_exp_f32_e32 v2, v2
	s_nop 0
	v_add_f32_e32 v2, 1.0, v2
	v_rcp_f32_e32 v183, v2
	v_mul_f32_e32 v2, 0xbfb8aa3b, v166
	v_exp_f32_e32 v2, v2
	v_pk_mul_f32 v[162:163], v[182:183], v[162:163]
	v_add_f32_e32 v2, 1.0, v2
	v_rcp_f32_e32 v182, v2
	v_mul_f32_e32 v2, 0xbfb8aa3b, v167
	v_exp_f32_e32 v2, v2
	s_nop 0
	v_add_f32_e32 v2, 1.0, v2
	v_rcp_f32_e32 v183, v2
	s_nop 0
	v_pk_mul_f32 v[166:167], v[182:183], v[166:167]
	global_load_dwordx2 v[182:183], v[68:69], off offset:208
	s_waitcnt vmcnt(0) lgkmcnt(0)
	v_lshlrev_b32_e32 v188, 16, v182
	v_mul_f32_e32 v2, 0xbfb8aa3b, v188
	v_exp_f32_e32 v2, v2
	v_and_b32_e32 v189, 0xffff0000, v182
	v_lshlrev_b32_e32 v182, 16, v183
	v_and_b32_e32 v183, 0xffff0000, v183
	v_add_f32_e32 v2, 1.0, v2
	v_rcp_f32_e32 v190, v2
	v_mul_f32_e32 v2, 0xbfb8aa3b, v189
	v_exp_f32_e32 v2, v2
	s_nop 0
	v_add_f32_e32 v2, 1.0, v2
	v_rcp_f32_e32 v191, v2
	v_mul_f32_e32 v2, 0xbfb8aa3b, v182
	v_exp_f32_e32 v2, v2
	v_pk_mul_f32 v[198:199], v[190:191], v[188:189]
	v_add_f32_e32 v2, 1.0, v2
	v_rcp_f32_e32 v188, v2
	v_mul_f32_e32 v2, 0xbfb8aa3b, v183
	v_exp_f32_e32 v2, v2
	s_nop 0
	v_add_f32_e32 v2, 1.0, v2
	v_rcp_f32_e32 v189, v2
	v_add_f32_e32 v2, v88, v89
	v_add_f32_e32 v2, v86, v2
	v_add_f32_e32 v2, v87, v2
	v_add_f32_e32 v2, v96, v2
	v_pk_mul_f32 v[200:201], v[188:189], v[182:183]
	global_load_dwordx2 v[182:183], v[68:69], off offset:224
	v_add_f32_e32 v2, v97, v2
	v_add_f32_e32 v2, v94, v2
	v_add_f32_e32 v2, v95, v2
	v_add_f32_e32 v2, v116, v2
	v_add_f32_e32 v2, v117, v2
	v_add_f32_e32 v2, v112, v2
	v_add_f32_e32 v2, v113, v2
	v_add_f32_e32 v2, v124, v2
	v_add_f32_e32 v2, v125, v2
	v_add_f32_e32 v2, v122, v2
	v_add_f32_e32 v2, v123, v2
	v_add_f32_e32 v2, v132, v2
	v_add_f32_e32 v2, v133, v2
	v_add_f32_e32 v2, v130, v2
	v_add_f32_e32 v2, v131, v2
	v_add_f32_e32 v2, v140, v2
	v_add_f32_e32 v2, v141, v2
	v_add_f32_e32 v2, v138, v2
	v_add_f32_e32 v2, v139, v2
	v_add_f32_e32 v2, v150, v2
	v_add_f32_e32 v2, v151, v2
	v_add_f32_e32 v2, v146, v2
	v_add_f32_e32 v2, v147, v2
	v_add_f32_e32 v2, v158, v2
	v_add_f32_e32 v2, v159, v2
	v_add_f32_e32 v2, v156, v2
	v_add_f32_e32 v2, v157, v2
	v_add_f32_e32 v2, v168, v2
	v_add_f32_e32 v2, v169, v2
	v_add_f32_e32 v2, v164, v2
	v_add_f32_e32 v2, v165, v2
	v_add_f32_e32 v2, v172, v2
	v_add_f32_e32 v2, v173, v2
	v_add_f32_e32 v2, v170, v2
	v_add_f32_e32 v2, v171, v2
	v_add_f32_e32 v2, v176, v2
	v_add_f32_e32 v2, v177, v2
	v_add_f32_e32 v2, v174, v2
	v_add_f32_e32 v2, v175, v2
	v_add_f32_e32 v2, v180, v2
	v_add_f32_e32 v2, v181, v2
	v_add_f32_e32 v2, v178, v2
	v_add_f32_e32 v2, v179, v2
	v_add_f32_e32 v2, v196, v2
	v_add_f32_e32 v2, v197, v2
	v_add_f32_e32 v2, v194, v2
	v_add_f32_e32 v2, v195, v2
	v_add_f32_e32 v2, v186, v2
	v_add_f32_e32 v2, v187, v2
	v_add_f32_e32 v2, v184, v2
	v_add_f32_e32 v2, v185, v2
	v_add_f32_e32 v2, v78, v2
	v_add_f32_e32 v2, v79, v2
	v_add_f32_e32 v2, v72, v2
	v_add_f32_e32 v2, v73, v2
	v_add_f32_e32 v2, v74, v2
	v_add_f32_e32 v2, v75, v2
	v_add_f32_e32 v2, v76, v2
	v_add_f32_e32 v2, v77, v2
	ds_bpermute_b32 v1, v1, v2
	s_waitcnt lgkmcnt(0)
	v_add_f32_e32 v1, v2, v1
	v_fmamk_f32 v1, v1, 0x3c000000, v241
	v_cmp_gt_f32_e32 vcc, s25, v1
	v_mul_f32_e32 v2, 0x4b800000, v1
	s_nop 0
	v_cndmask_b32_e32 v1, v1, v2, vcc
	v_rsq_f32_e32 v1, v1
	s_nop 0
	v_mul_f32_e32 v2, 0x45800000, v1
	v_cndmask_b32_e32 v2, v1, v2, vcc
	v_pk_mul_f32 v[4:5], v[4:5], v[2:3] op_sel_hi:[1,0]
	v_pk_mul_f32 v[6:7], v[6:7], v[2:3] op_sel_hi:[1,0]
	v_pk_mul_f32 v[4:5], v[162:163], v[4:5]
	v_pk_mul_f32 v[6:7], v[166:167], v[6:7]
	v_cvt_pk_bf16_f32 v4, v4, v5
	v_cvt_pk_bf16_f32 v5, v6, v7
	global_store_dwordx2 v[18:19], v[4:5], off offset:192
	v_pk_mul_f32 v[4:5], v[8:9], v[2:3] op_sel_hi:[1,0]
	v_pk_mul_f32 v[6:7], v[10:11], v[2:3] op_sel_hi:[1,0]
	v_pk_mul_f32 v[4:5], v[198:199], v[4:5]
	v_pk_mul_f32 v[6:7], v[200:201], v[6:7]
	v_cvt_pk_bf16_f32 v4, v4, v5
	v_cvt_pk_bf16_f32 v5, v6, v7
	global_store_dwordx2 v[18:19], v[4:5], off offset:208
	s_waitcnt vmcnt(0)
	v_lshlrev_b32_e32 v4, 16, v182
	v_mul_f32_e32 v1, 0xbfb8aa3b, v4
	v_exp_f32_e32 v1, v1
	v_and_b32_e32 v5, 0xffff0000, v182
	v_pk_mul_f32 v[8:9], v[12:13], v[2:3] op_sel_hi:[1,0]
	v_pk_mul_f32 v[10:11], v[70:71], v[2:3] op_sel_hi:[1,0]
	v_add_f32_e32 v1, 1.0, v1
	v_rcp_f32_e32 v6, v1
	v_mul_f32_e32 v1, 0xbfb8aa3b, v5
	v_exp_f32_e32 v1, v1
	v_pk_mul_f32 v[52:53], v[52:53], v[2:3] op_sel_hi:[1,0]
	v_pk_mul_f32 v[54:55], v[54:55], v[2:3] op_sel_hi:[1,0]
	v_pk_mul_f32 v[52:53], v[80:81], v[52:53]
	v_add_f32_e32 v1, 1.0, v1
	v_rcp_f32_e32 v7, v1
	v_pk_mul_f32 v[54:55], v[84:85], v[54:55]
	v_pk_mul_f32 v[36:37], v[36:37], v[2:3] op_sel_hi:[1,0]
	v_pk_mul_f32 v[38:39], v[38:39], v[2:3] op_sel_hi:[1,0]
	v_pk_mul_f32 v[4:5], v[6:7], v[4:5]
	v_lshlrev_b32_e32 v6, 16, v183
	v_mul_f32_e32 v1, 0xbfb8aa3b, v6
	v_exp_f32_e32 v1, v1
	v_and_b32_e32 v7, 0xffff0000, v183
	v_pk_mul_f32 v[4:5], v[4:5], v[8:9]
	v_pk_mul_f32 v[20:21], v[20:21], v[2:3] op_sel_hi:[1,0]
	v_add_f32_e32 v1, 1.0, v1
	v_rcp_f32_e32 v8, v1
	v_mul_f32_e32 v1, 0xbfb8aa3b, v7
	v_exp_f32_e32 v1, v1
	v_cvt_pk_bf16_f32 v4, v4, v5
	v_pk_mul_f32 v[22:23], v[22:23], v[2:3] op_sel_hi:[1,0]
	v_cvt_pk_bf16_f32 v52, v52, v53
	v_add_f32_e32 v1, 1.0, v1
	v_rcp_f32_e32 v9, v1
	v_cvt_pk_bf16_f32 v53, v54, v55
	v_add_co_u32_e32 v54, vcc, s2, v82
	v_pk_mul_f32 v[6:7], v[8:9], v[6:7]
	v_pk_mul_f32 v[36:37], v[106:107], v[36:37]
	v_pk_mul_f32 v[6:7], v[6:7], v[10:11]
	v_pk_mul_f32 v[10:11], v[16:17], v[2:3] op_sel_hi:[1,0]
	v_cvt_pk_bf16_f32 v5, v6, v7
	global_store_dwordx2 v[18:19], v[4:5], off offset:224
	global_load_dwordx2 v[4:5], v[68:69], off offset:240
	v_pk_mul_f32 v[38:39], v[108:109], v[38:39]
	v_pk_mul_f32 v[20:21], v[134:135], v[20:21]
	v_pk_mul_f32 v[22:23], v[136:137], v[22:23]
	v_addc_co_u32_e32 v55, vcc, 0, v83, vcc
	v_cvt_pk_bf16_f32 v36, v36, v37
	v_cvt_pk_bf16_f32 v37, v38, v39
	v_cvt_pk_bf16_f32 v20, v20, v21
	v_cvt_pk_bf16_f32 v21, v22, v23
	global_store_dwordx2 v[54:55], v[52:53], off
	v_pk_mul_f32 v[52:53], v[56:57], v[2:3] op_sel_hi:[1,0]
	v_pk_mul_f32 v[54:55], v[58:59], v[2:3] op_sel_hi:[1,0]
	global_store_dwordx2 v[18:19], v[36:37], off offset:64
	v_pk_mul_f32 v[36:37], v[40:41], v[2:3] op_sel_hi:[1,0]
	v_pk_mul_f32 v[38:39], v[42:43], v[2:3] op_sel_hi:[1,0]
	global_store_dwordx2 v[18:19], v[20:21], off offset:128
	v_pk_mul_f32 v[20:21], v[24:25], v[2:3] op_sel_hi:[1,0]
	v_pk_mul_f32 v[22:23], v[26:27], v[2:3] op_sel_hi:[1,0]
	v_pk_mul_f32 v[52:53], v[90:91], v[52:53]
	v_pk_mul_f32 v[54:55], v[92:93], v[54:55]
	v_pk_mul_f32 v[36:37], v[110:111], v[36:37]
	v_pk_mul_f32 v[38:39], v[114:115], v[38:39]
	v_pk_mul_f32 v[20:21], v[142:143], v[20:21]
	v_pk_mul_f32 v[22:23], v[144:145], v[22:23]
	v_cvt_pk_bf16_f32 v52, v52, v53
	v_cvt_pk_bf16_f32 v53, v54, v55
	v_cvt_pk_bf16_f32 v36, v36, v37
	v_cvt_pk_bf16_f32 v37, v38, v39
	v_cvt_pk_bf16_f32 v20, v20, v21
	v_cvt_pk_bf16_f32 v21, v22, v23
	global_store_dwordx2 v[18:19], v[52:53], off offset:16
	v_pk_mul_f32 v[52:53], v[60:61], v[2:3] op_sel_hi:[1,0]
	v_pk_mul_f32 v[54:55], v[62:63], v[2:3] op_sel_hi:[1,0]
	global_store_dwordx2 v[18:19], v[36:37], off offset:80
	v_pk_mul_f32 v[36:37], v[44:45], v[2:3] op_sel_hi:[1,0]
	v_pk_mul_f32 v[38:39], v[46:47], v[2:3] op_sel_hi:[1,0]
	global_store_dwordx2 v[18:19], v[20:21], off offset:144
	v_pk_mul_f32 v[20:21], v[28:29], v[2:3] op_sel_hi:[1,0]
	v_pk_mul_f32 v[22:23], v[30:31], v[2:3] op_sel_hi:[1,0]
	v_pk_mul_f32 v[52:53], v[98:99], v[52:53]
	v_pk_mul_f32 v[54:55], v[100:101], v[54:55]
	v_pk_mul_f32 v[36:37], v[118:119], v[36:37]
	v_pk_mul_f32 v[38:39], v[120:121], v[38:39]
	v_pk_mul_f32 v[20:21], v[148:149], v[20:21]
	v_pk_mul_f32 v[22:23], v[152:153], v[22:23]
	v_cvt_pk_bf16_f32 v52, v52, v53
	v_cvt_pk_bf16_f32 v53, v54, v55
	v_cvt_pk_bf16_f32 v36, v36, v37
	v_cvt_pk_bf16_f32 v37, v38, v39
	v_cvt_pk_bf16_f32 v20, v20, v21
	v_cvt_pk_bf16_f32 v21, v22, v23
	global_store_dwordx2 v[18:19], v[52:53], off offset:32
	v_pk_mul_f32 v[52:53], v[64:65], v[2:3] op_sel_hi:[1,0]
	v_pk_mul_f32 v[54:55], v[66:67], v[2:3] op_sel_hi:[1,0]
	global_store_dwordx2 v[18:19], v[36:37], off offset:96
	v_pk_mul_f32 v[36:37], v[48:49], v[2:3] op_sel_hi:[1,0]
	v_pk_mul_f32 v[38:39], v[50:51], v[2:3] op_sel_hi:[1,0]
	global_store_dwordx2 v[18:19], v[20:21], off offset:160
	v_pk_mul_f32 v[20:21], v[32:33], v[2:3] op_sel_hi:[1,0]
	v_pk_mul_f32 v[22:23], v[34:35], v[2:3] op_sel_hi:[1,0]
	v_pk_mul_f32 v[52:53], v[102:103], v[52:53]
	v_pk_mul_f32 v[54:55], v[104:105], v[54:55]
	v_pk_mul_f32 v[36:37], v[126:127], v[36:37]
	v_pk_mul_f32 v[38:39], v[128:129], v[38:39]
	v_pk_mul_f32 v[20:21], v[154:155], v[20:21]
	v_pk_mul_f32 v[22:23], v[160:161], v[22:23]
	v_cvt_pk_bf16_f32 v52, v52, v53
	v_cvt_pk_bf16_f32 v53, v54, v55
	v_cvt_pk_bf16_f32 v36, v36, v37
	v_cvt_pk_bf16_f32 v37, v38, v39
	v_cvt_pk_bf16_f32 v20, v20, v21
	v_cvt_pk_bf16_f32 v21, v22, v23
	s_mov_b64 s[2:3], 0
	global_store_dwordx2 v[18:19], v[52:53], off offset:48
	global_store_dwordx2 v[18:19], v[36:37], off offset:112
	global_store_dwordx2 v[18:19], v[20:21], off offset:176
	s_waitcnt vmcnt(0) lgkmcnt(0)
	v_lshlrev_b32_e32 v6, 16, v4
	v_mul_f32_e32 v1, 0xbfb8aa3b, v6
	v_exp_f32_e32 v1, v1
	v_and_b32_e32 v7, 0xffff0000, v4
	v_add_f32_e32 v1, 1.0, v1
	v_rcp_f32_e32 v8, v1
	v_mul_f32_e32 v1, 0xbfb8aa3b, v7
	v_exp_f32_e32 v1, v1
	s_nop 0
	v_add_f32_e32 v1, 1.0, v1
	v_rcp_f32_e32 v9, v1
	s_nop 0
	v_pk_mul_f32 v[6:7], v[8:9], v[6:7]
	s_nop 0
	v_pk_mul_f32 v[6:7], v[6:7], v[10:11]
	v_pk_mul_f32 v[10:11], v[14:15], v[2:3] op_sel_hi:[1,0]
	v_cvt_pk_bf16_f32 v4, v6, v7
	v_lshlrev_b32_e32 v6, 16, v5
	v_mul_f32_e32 v1, 0xbfb8aa3b, v6
	v_exp_f32_e32 v1, v1
	v_and_b32_e32 v7, 0xffff0000, v5
	v_add_f32_e32 v1, 1.0, v1
	v_rcp_f32_e32 v8, v1
	v_mul_f32_e32 v1, 0xbfb8aa3b, v7
	v_exp_f32_e32 v1, v1
	s_nop 0
	v_add_f32_e32 v1, 1.0, v1
	v_rcp_f32_e32 v9, v1
	s_nop 0
	v_pk_mul_f32 v[6:7], v[8:9], v[6:7]
	s_nop 0
	v_pk_mul_f32 v[6:7], v[6:7], v[10:11]
	s_nop 0
	v_cvt_pk_bf16_f32 v5, v6, v7
	global_store_dwordx2 v[18:19], v[4:5], off offset:240
